# T3a stage I: P / Q' record tiles stored as two 16-byte pieces per lane (half-waves exchanged with v_permlane32_swap) instead of four interleaved 8-byte stores
# speedup vs baseline: 1.0155x; 1.0155x over previous
; __device__ __forceinline__ void phase1(const int WID_, const In& I, char* lds) {
;     ...
;         const int lane = lane_id(), tid = wv * 64 + lane;
;         const int c = item & 127, h = (item >> 7) & 7, b = item >> 10;
;         char* out = I.items + (size_t)item * ITEM_BYTES;
;         const int s = tid >> 3, cg = tid & 7, ch0 = h * 64 + cg * 8, t = c * 64 + s; const size_t m = (size_t)b * S + t;
;         float r_[8], kp_[8], v_[8], kk_[8], b_[8];
;         {
;             const uint4 z4 = make_uint4(0, 0, 0, 0);
;             const uint4 gr = nx_r, gk = nx_k, gv = nx_v, qr = t > 0 ? nx_qr : z4, qk = t > 0 ? nx_qk : z4, qv = t > 0 ? nx_qv : z4, ga = nx_a, gl = nx_l;
;             typedef _Float16 h8_t __attribute__((ext_vector_type(8)));
;             const h8_t c_mr = *(const h8_t*)(CST + ch0), c_mk = *(const h8_t*)(CST + 512 + ch0), c_mv = *(const h8_t*)(CST + 1024 + ch0), c_kk = *(const h8_t*)(CST + 1536 + ch0), c_ka = *(const h8_t*)(CST + 2048 + ch0), c_rk = *(const h8_t*)(CST + 2560 + ch0);
;             float mur[8], muk[8], muv[8], ckk[8], cka[8], crk[8];
; #pragma unroll
;             for (int e = 0; e < 8; ++e) { mur[e] = (float)c_mr[e]; muk[e] = (float)c_mk[e]; muv[e] = (float)c_mv[e]; ckk[e] = (float)c_kk[e]; cka[e] = (float)c_ka[e]; crk[e] = (float)c_rk[e]; }
;             const unsigned wr[4] = {gr.x, gr.y, gr.z, gr.w}, wk[4] = {gk.x, gk.y, gk.z, gk.w}, wv4[4] = {gv.x, gv.y, gv.z, gv.w};
;             const unsigned pr[4] = {qr.x, qr.y, qr.z, qr.w}, pk[4] = {qk.x, qk.y, qk.z, qk.w}, pv[4] = {qv.x, qv.y, qv.z, qv.w};
;             const unsigned wa[4] = {ga.x, ga.y, ga.z, ga.w}, wl[4] = {gl.x, gl.y, gl.z, gl.w};
;             float ss = 0.f, rk = 0.f, a_[8];
; #pragma unroll
;             for (int e = 0; e < 8; ++e) { const int w_ = e >> 1; const bool hi = e & 1;
;                 auto ex = [&](unsigned u) { return hi ? __builtin_bit_cast(float, u & 0xffff0000u) : __builtin_bit_cast(float, u << 16); };
;                 float x = ex(wr[w_]); r_[e] = x + (ex(pr[w_]) - x) * mur[e];
;                 x = ex(wk[w_]); const float k = x + (ex(pk[w_]) - x) * muk[e];
;     ...
;             const bool frag = kind < 2;
;             *(uint2*)(dbase + 0) = w[0];
;             *(uint2*)(dbase + (frag ? 128 : 8)) = w[1];
;             *(uint2*)(dbase + (frag ? 1024 : 16)) = w[2];
;             *(uint2*)(dbase + (frag ? 1152 : 24)) = w[3];
;         }
.LBB0_1413:
	v_cvt_pk_bf16_f32 v0, v0, v1
	v_cvt_pk_bf16_f32 v1, v2, v3
	v_cvt_pk_bf16_f32 v4, v4, v5
	v_cvt_pk_bf16_f32 v5, v6, v7
	v_cvt_pk_bf16_f32 v2, v8, v9
	v_cvt_pk_bf16_f32 v3, v10, v11
	v_cvt_pk_bf16_f32 v6, v12, v13
	v_cvt_pk_bf16_f32 v7, v14, v15
	v_mbcnt_lo_u32_b32 v8, -1, 0
	v_mbcnt_hi_u32_b32 v8, -1, v8
	v_and_b32_e32 v8, 32, v8
	v_lshrrev_b32_e32 v9, 2, v8
	v_sub_u32_e32 v68, v8, v9
	v_permlane32_swap_b32_e32 v0, v2
	v_permlane32_swap_b32_e32 v1, v3
	v_permlane32_swap_b32_e32 v4, v6
	v_permlane32_swap_b32_e32 v5, v7
	v_lshl_add_u64 v[72:73], v[72:73], 0, v[68:69]
	global_store_dwordx4 v[72:73], v[0:3], off
	global_store_dwordx4 v[72:73], v[4:7], off offset:16
	s_waitcnt lgkmcnt(0)
	s_cmpk_lt_i32 s33, 0x2000
	s_mov_b32 s40, s33
	s_cbranch_scc0 .LBB0_1473
.LBB0_1414:
	s_waitcnt lgkmcnt(1)
	v_mbcnt_lo_u32_b32 v58, -1, 0
	v_mbcnt_hi_u32_b32 v58, -1, v58
	s_bfe_u32 s4, s40, 0x30007
	v_and_b32_e32 v61, 7, v58
	v_lshlrev_b32_e32 v0, 4, v61
	v_lshl_or_b32 v0, s4, 7, v0
	v_add_u32_e32 v4, 0, v0
	v_add_u32_e32 v0, 0x21c00, v4
	ds_read_b128 v[64:67], v0
	v_add_u32_e32 v59, s86, v58
	s_lshl_b32 s0, s40, 6
	v_ashrrev_i32_e32 v60, 3, v59
	s_and_b32 s0, s0, 0x1fc0
	v_add_u32_e32 v5, 0x22800, v4
	s_waitcnt lgkmcnt(1)
	v_add_u32_e32 v52, s0, v60
	ds_read_b128 v[8:11], v5
	v_add_u32_e32 v0, 0x22000, v4
	v_cmp_lt_i32_e32 vcc, 0, v52
	ds_read_b128 v[70:73], v0
	v_add_u32_e32 v5, 0x22c00, v4
	s_waitcnt vmcnt(9)
	v_cndmask_b32_e32 v55, 0, v48, vcc
	v_cndmask_b32_e32 v63, 0, v50, vcc
	ds_read_b128 v[78:81], v5
	v_cndmask_b32_e32 v74, 0, v49, vcc
	v_cndmask_b32_e32 v90, 0, v51, vcc
	s_waitcnt vmcnt(6)
	v_lshlrev_b32_e32 v50, 16, v41
	v_lshlrev_b32_e32 v48, 16, v40
	v_and_b32_e32 v51, 0xffff0000, v41
	v_and_b32_e32 v49, 0xffff0000, v40
	s_waitcnt lgkmcnt(3)
	v_cvt_f32_f16_e32 v40, v64
	v_cvt_f32_f16_sdwa v41, v64 dst_sel:DWORD dst_unused:UNUSED_PAD src0_sel:WORD_1
	v_cndmask_b32_e32 v15, 0, v44, vcc
	v_lshlrev_b32_e32 v12, 8, v60
	v_lshlrev_b32_e32 v13, 5, v61
	v_add3_u32 v62, s77, v12, v13
	v_lshlrev_b32_e32 v12, 16, v36
	v_lshlrev_b32_e32 v14, 16, v15
	v_and_b32_e32 v13, 0xffff0000, v36
	v_and_b32_e32 v15, 0xffff0000, v15
	v_pk_add_f32 v[14:15], v[14:15], v[12:13] neg_lo:[0,1] neg_hi:[0,1]
	v_cndmask_b32_e32 v53, 0, v46, vcc
	v_pk_fma_f32 v[12:13], v[14:15], v[40:41], v[12:13]
	s_waitcnt lgkmcnt(1)
	v_cvt_f32_f16_e32 v14, v70
	v_cvt_f32_f16_sdwa v15, v70 dst_sel:DWORD dst_unused:UNUSED_PAD src0_sel:WORD_1
	s_waitcnt lgkmcnt(0)
; template <int CTRL> __device__ __forceinline__ float dpp16(float x) { return __builtin_bit_cast(float, __builtin_amdgcn_update_dpp(0, __builtin_bit_cast(int, x), CTRL, 0xf, 0xf, true)); }
; __device__ __forceinline__ void phase1(const int WID_, const In& I, char* lds) {
;     ...
;             const h8_t c_mr = *(const h8_t*)(CST + ch0), c_mk = *(const h8_t*)(CST + 512 + ch0), c_mv = *(const h8_t*)(CST + 1024 + ch0), c_kk = *(const h8_t*)(CST + 1536 + ch0), c_ka = *(const h8_t*)(CST + 2048 + ch0), c_rk = *(const h8_t*)(CST + 2560 + ch0);
;             float mur[8], muk[8], muv[8], ckk[8], cka[8], crk[8];
; #pragma unroll
;             for (int e = 0; e < 8; ++e) { mur[e] = (float)c_mr[e]; muk[e] = (float)c_mk[e]; muv[e] = (float)c_mv[e]; ckk[e] = (float)c_kk[e]; cka[e] = (float)c_ka[e]; crk[e] = (float)c_rk[e]; }
;             const unsigned wr[4] = {gr.x, gr.y, gr.z, gr.w}, wk[4] = {gk.x, gk.y, gk.z, gk.w}, wv4[4] = {gv.x, gv.y, gv.z, gv.w};
;             const unsigned pr[4] = {qr.x, qr.y, qr.z, qr.w}, pk[4] = {qk.x, qk.y, qk.z, qk.w}, pv[4] = {qv.x, qv.y, qv.z, qv.w};
;             const unsigned wa[4] = {ga.x, ga.y, ga.z, ga.w}, wl[4] = {gl.x, gl.y, gl.z, gl.w};
;             float ss = 0.f, rk = 0.f, a_[8];
; #pragma unroll
;             for (int e = 0; e < 8; ++e) { const int w_ = e >> 1; const bool hi = e & 1;
;                 auto ex = [&](unsigned u) { return hi ? __builtin_bit_cast(float, u & 0xffff0000u) : __builtin_bit_cast(float, u << 16); };
;                 float x = ex(wr[w_]); r_[e] = x + (ex(pr[w_]) - x) * mur[e];
;                 x = ex(wk[w_]); const float k = x + (ex(pk[w_]) - x) * muk[e];
;                 x = ex(wv4[w_]); v_[e] = x + (ex(pv[w_]) - x) * muv[e];
;                 a_[e] = ex(wa[w_]); kk_[e] = k * ckk[e]; ss += kk_[e] * kk_[e];
;                 kp_[e] = k * (1.f + (a_[e] - 1.f) * cka[e]); rk += r_[e] * kp_[e] * crk[e];
;                 G[s * 64 + cg * 8 + e] = ex(wl[w_]); }
;             ss += dpp16<0xB1>(ss); ss += dpp16<0x4E>(ss); ss += dpp16<0x141>(ss);
;             const float inv = 1.f / fmaxf(sqrtf(ss), 1e-12f);
; #pragma unroll
;             for (int e = 0; e < 8; ++e) { kk_[e] *= inv; b_[e] = kk_[e] * a_[e]; }
;             rk += dpp16<0xB1>(rk); rk += dpp16<0x4E>(rk); rk += dpp16<0x141>(rk);
;             if (cg == 0) I.RK[m * 8 + h] = rk;
	v_cvt_f32_f16_e32 v40, v78
	v_cvt_f32_f16_sdwa v41, v78 dst_sel:DWORD dst_unused:UNUSED_PAD src0_sel:WORD_1
	v_cndmask_b32_e32 v88, 0, v47, vcc
	v_lshlrev_b32_e32 v46, 16, v28
	v_lshlrev_b32_e32 v54, 16, v55
	v_and_b32_e32 v47, 0xffff0000, v28
	v_and_b32_e32 v55, 0xffff0000, v55
	v_cndmask_b32_e32 v68, 0, v45, vcc
	v_lshlrev_b32_e32 v44, 16, v32
	v_lshlrev_b32_e32 v84, 16, v43
	v_lshlrev_b32_e32 v82, 16, v42
	v_and_b32_e32 v85, 0xffff0000, v43
	v_and_b32_e32 v83, 0xffff0000, v42
	v_and_b32_e32 v45, 0xffff0000, v32
	v_pk_add_f32 v[42:43], v[54:55], v[46:47] neg_lo:[0,1] neg_hi:[0,1]
	v_cvt_f32_f16_e32 v64, v65
	v_cvt_f32_f16_sdwa v65, v65 dst_sel:DWORD dst_unused:UNUSED_PAD src0_sel:WORD_1
	v_pk_fma_f32 v[56:57], v[42:43], v[14:15], v[46:47]
	v_pk_add_f32 v[14:15], v[44:45], -1.0 op_sel_hi:[1,0]
	v_lshlrev_b32_e32 v36, 16, v37
	v_pk_fma_f32 v[14:15], v[14:15], v[40:41], 1.0 op_sel_hi:[1,1,0]
	v_lshlrev_b32_e32 v40, 16, v68
	v_and_b32_e32 v37, 0xffff0000, v37
	v_and_b32_e32 v41, 0xffff0000, v68
	v_lshlrev_b32_e32 v42, 16, v33
	v_pk_add_f32 v[40:41], v[40:41], v[36:37] neg_lo:[0,1] neg_hi:[0,1]
	v_and_b32_e32 v43, 0xffff0000, v33
	v_cvt_f32_f16_e32 v32, v71
	v_cvt_f32_f16_sdwa v33, v71 dst_sel:DWORD dst_unused:UNUSED_PAD src0_sel:WORD_1
	v_pk_fma_f32 v[36:37], v[40:41], v[64:65], v[36:37]
	v_cvt_f32_f16_e32 v40, v79
	v_cvt_f32_f16_sdwa v41, v79 dst_sel:DWORD dst_unused:UNUSED_PAD src0_sel:WORD_1
	v_lshlrev_b32_e32 v28, 16, v29
	v_lshlrev_b32_e32 v46, 16, v74
	v_and_b32_e32 v29, 0xffff0000, v29
	v_and_b32_e32 v47, 0xffff0000, v74
	v_pk_add_f32 v[46:47], v[46:47], v[28:29] neg_lo:[0,1] neg_hi:[0,1]
	v_cvt_f32_f16_e32 v86, v66
	v_cvt_f32_f16_sdwa v87, v66 dst_sel:DWORD dst_unused:UNUSED_PAD src0_sel:WORD_1
	v_pk_fma_f32 v[64:65], v[46:47], v[32:33], v[28:29]
	v_pk_add_f32 v[28:29], v[42:43], -1.0 op_sel_hi:[1,0]
	v_lshlrev_b32_e32 v32, 16, v38
	v_pk_fma_f32 v[28:29], v[28:29], v[40:41], 1.0 op_sel_hi:[1,1,0]
	v_lshlrev_b32_e32 v40, 16, v53
	v_and_b32_e32 v33, 0xffff0000, v38
	v_and_b32_e32 v41, 0xffff0000, v53
	v_pk_add_f32 v[40:41], v[40:41], v[32:33] neg_lo:[0,1] neg_hi:[0,1]
	v_lshlrev_b32_e32 v74, 16, v30
	v_pk_fma_f32 v[32:33], v[40:41], v[86:87], v[32:33]
	v_cvt_f32_f16_e32 v40, v72
	v_cvt_f32_f16_sdwa v41, v72 dst_sel:DWORD dst_unused:UNUSED_PAD src0_sel:WORD_1
	v_cvt_f32_f16_e32 v86, v80
	v_cvt_f32_f16_sdwa v87, v80 dst_sel:DWORD dst_unused:UNUSED_PAD src0_sel:WORD_1
	v_lshlrev_b32_e32 v78, 16, v63
	v_and_b32_e32 v75, 0xffff0000, v30
	v_and_b32_e32 v79, 0xffff0000, v63
	v_lshlrev_b32_e32 v46, 16, v34
	v_and_b32_e32 v47, 0xffff0000, v34
	v_pk_add_f32 v[78:79], v[78:79], v[74:75] neg_lo:[0,1] neg_hi:[0,1]
	v_cvt_f32_f16_e32 v72, v73
	v_cvt_f32_f16_sdwa v73, v73 dst_sel:DWORD dst_unused:UNUSED_PAD src0_sel:WORD_1
	v_add_u32_e32 v0, 0x22400, v4
	v_add_u32_e32 v4, 0x23000, v4
	v_pk_fma_f32 v[74:75], v[78:79], v[40:41], v[74:75]
	v_pk_add_f32 v[40:41], v[46:47], -1.0 op_sel_hi:[1,0]
	v_cvt_f32_f16_e32 v80, v81
	v_cvt_f32_f16_sdwa v81, v81 dst_sel:DWORD dst_unused:UNUSED_PAD src0_sel:WORD_1
	ds_read_b128 v[0:3], v0
	ds_read_b128 v[4:7], v4
	v_pk_fma_f32 v[40:41], v[40:41], v[86:87], 1.0 op_sel_hi:[1,1,0]
	v_lshlrev_b32_e32 v86, 16, v88
	v_lshlrev_b32_e32 v30, 16, v31
	v_lshlrev_b32_e32 v66, 16, v90
	v_and_b32_e32 v87, 0xffff0000, v88
	v_cvt_f32_f16_e32 v88, v67
	v_cvt_f32_f16_sdwa v89, v67 dst_sel:DWORD dst_unused:UNUSED_PAD src0_sel:WORD_1
	v_and_b32_e32 v31, 0xffff0000, v31
	v_and_b32_e32 v67, 0xffff0000, v90
	ds_write_b128 v62, v[82:85] offset:16
	ds_write_b128 v62, v[48:51]
	v_cvt_f32_f16_e32 v50, v10
	v_cvt_f32_f16_sdwa v51, v10 dst_sel:DWORD dst_unused:UNUSED_PAD src0_sel:WORD_1
	v_lshlrev_b32_e32 v34, 16, v35
	v_and_b32_e32 v35, 0xffff0000, v35
	v_pk_add_f32 v[66:67], v[66:67], v[30:31] neg_lo:[0,1] neg_hi:[0,1]
	v_cvt_f32_f16_e32 v48, v11
	v_pk_fma_f32 v[66:67], v[66:67], v[72:73], v[30:31]
	v_pk_add_f32 v[30:31], v[34:35], -1.0 op_sel_hi:[1,0]
	v_cvt_f32_f16_sdwa v49, v11 dst_sel:DWORD dst_unused:UNUSED_PAD src0_sel:WORD_1
	v_pk_fma_f32 v[30:31], v[30:31], v[80:81], 1.0 op_sel_hi:[1,1,0]
	v_cvt_f32_f16_e32 v80, v8
	v_cvt_f32_f16_sdwa v81, v8 dst_sel:DWORD dst_unused:UNUSED_PAD src0_sel:WORD_1
	v_pk_mul_f32 v[10:11], v[74:75], v[50:51]
	v_cvt_f32_f16_e32 v50, v9
	v_cvt_f32_f16_sdwa v51, v9 dst_sel:DWORD dst_unused:UNUSED_PAD src0_sel:WORD_1
	v_pk_mul_f32 v[8:9], v[56:57], v[80:81]
	v_pk_mul_f32 v[14:15], v[14:15], v[56:57]
	v_pk_mul_f32 v[56:57], v[8:9], v[8:9]
	v_pk_mul_f32 v[50:51], v[64:65], v[50:51]
	v_pk_mul_f32 v[28:29], v[28:29], v[64:65]
	v_pk_mul_f32 v[64:65], v[50:51], v[50:51]
	v_add_f32_e32 v53, v56, v57
	v_add_f32_e32 v53, v64, v53
	v_pk_mul_f32 v[40:41], v[40:41], v[74:75]
	v_pk_mul_f32 v[74:75], v[10:11], v[10:11]
	v_add_f32_e32 v53, v65, v53
	v_pk_mul_f32 v[48:49], v[66:67], v[48:49]
	v_add_f32_e32 v53, v74, v53
	v_pk_mul_f32 v[30:31], v[30:31], v[66:67]
	v_pk_mul_f32 v[66:67], v[48:49], v[48:49]
	v_add_f32_e32 v53, v75, v53
	v_add_f32_e32 v53, v66, v53
	v_add_f32_e32 v53, v67, v53
	v_pk_mul_f32 v[54:55], v[12:13], v[14:15]
	v_pk_mul_f32 v[70:71], v[36:37], v[28:29]
	v_add_f32_dpp v53, v53, v53 quad_perm:[1,0,3,2] row_mask:0xf bank_mask:0xf bound_ctrl:1
	v_lshlrev_b32_e32 v38, 16, v39
	v_and_b32_e32 v39, 0xffff0000, v39
	v_add_f32_dpp v56, v53, v53 quad_perm:[2,3,0,1] row_mask:0xf bank_mask:0xf bound_ctrl:1
	s_waitcnt lgkmcnt(2)
	v_fma_mix_f32 v53, v54, v4, 0 op_sel_hi:[0,1,0]
	v_fma_mix_f32 v4, v55, v4, v53 op_sel:[0,1,0] op_sel_hi:[0,1,0]
	v_fma_mix_f32 v4, v70, v5, v4 op_sel_hi:[0,1,0]
	v_pk_mul_f32 v[78:79], v[32:33], v[40:41]
	v_pk_add_f32 v[86:87], v[86:87], v[38:39] neg_lo:[0,1] neg_hi:[0,1]
	v_fma_mix_f32 v4, v71, v5, v4 op_sel:[0,1,0] op_sel_hi:[0,1,0]
	v_pk_fma_f32 v[38:39], v[86:87], v[88:89], v[38:39]
	v_fma_mix_f32 v4, v78, v6, v4 op_sel_hi:[0,1,0]
	v_pk_mul_f32 v[72:73], v[38:39], v[30:31]
	v_fma_mix_f32 v4, v79, v6, v4 op_sel:[0,1,0] op_sel_hi:[0,1,0]
	v_fma_mix_f32 v4, v72, v7, v4 op_sel_hi:[0,1,0]
	v_fma_mix_f32 v4, v73, v7, v4 op_sel:[0,1,0] op_sel_hi:[0,1,0]
	v_mov_b32_dpp v57, v56 row_half_mirror row_mask:0xf bank_mask:0xf bound_ctrl:1
	v_cmp_eq_u32_e64 s[0:1], 0, v61
	v_add_f32_dpp v4, v4, v4 quad_perm:[1,0,3,2] row_mask:0xf bank_mask:0xf bound_ctrl:1
	s_nop 1
	v_add_f32_dpp v4, v4, v4 quad_perm:[2,3,0,1] row_mask:0xf bank_mask:0xf bound_ctrl:1
	s_nop 1
	v_mov_b32_dpp v5, v4 row_half_mirror row_mask:0xf bank_mask:0xf bound_ctrl:1
	s_and_saveexec_b64 s[6:7], s[0:1]
	s_cbranch_execz .LBB0_1416
	s_ashr_i32 s0, s40, 10
	s_ashr_i32 s1, s0, 31
	s_lshl_b64 s[0:1], s[0:1], 18
	v_ashrrev_i32_e32 v53, 31, v52
	s_add_u32 s0, s10, s0
	v_add_f32_e32 v6, v4, v5
	s_addc_u32 s1, s11, s1
	v_lshlrev_b64 v[4:5], 5, v[52:53]
	v_lshl_add_u64 v[4:5], s[0:1], 0, v[4:5]
	s_lshl_b32 s4, s4, 2
	v_lshl_add_u64 v[4:5], v[4:5], 0, s[4:5]
	global_store_dword v[4:5], v6, off
